# band attention near-tile bias: 16 LDS table reads issued as one batch into dedicated registers with counted lgkmcnt waits (was 5 serialized batches)
# baseline (speedup 1.0000x reference)
; #define LAS __attribute__((address_space(3)))
; #define MFMA32(a, b, c) __builtin_amdgcn_mfma_f32_32x32x16_bf16((a), (b), (c), 0, 0, 0)
; __device__ __forceinline__ void unit(LAS unsigned char* lds, const bf16* __restrict__ Q, const bf16* __restrict__ Kp, const bf16* __restrict__ VT, const float* __restrict__ rel, bf16* mix, float* ssa, int b, int h, int u) {
;     ...
;             bf16x8 kf0[4], kf1[4], vf0[4], vf1[4];
; #pragma unroll
;             for (int d0 = 0; d0 < 4; ++d0) { const LAS unsigned char* kp_ = lds + (kof[d0] + sbo); kf0[d0] = *(const LAS bf16x8*)kp_; kf1[d0] = *(const LAS bf16x8*)(kp_ + 4096); }
; #pragma unroll
;             for (int d0 = 0; d0 < 4; ++d0) { const LAS unsigned char* vp_ = lds + (vof[d0] + sbo); vf0[d0] = *(const LAS bf16x8*)vp_; vf1[d0] = *(const LAS bf16x8*)(vp_ + 4096); }
;             f32x16 p0 = MFMA32(kf0[0], qf[0], cfarv), p1 = MFMA32(kf1[0], qf[0], cfarv);
; #pragma unroll
;             for (int d0 = 1; d0 < 4; ++d0) { p0 = MFMA32(kf0[d0], qf[d0], p0); p1 = MFMA32(kf1[d0], qf[d0], p1); }
;             if (dj < 3) { const LAS float* tb = tab + (64 * dj + 32 * qh + r32 + 128 - 8 * hh - 55); asm volatile("" : "+v"(tb));
; #pragma unroll
;                 for (int r = 0; r < 16; ++r) { p0[r] += tb[55 - (16 * (r >> 3) + (r & 7))]; p1[r] += tb[23 - (16 * (r >> 3) + (r & 7))]; } }
.LBB5_985:
	s_add_i32 s36, s54, s55
	s_cmp_lt_i32 s36, 0
	s_cbranch_scc1 .LBB5_996
	s_mul_hi_u32 s36, s52, 0xaaaaaaab
	s_lshr_b32 s36, s36, 2
	s_mul_i32 s36, s36, 0x18000
	s_sub_i32 s36, s53, s36
	s_add_i32 s36, s36, 0
	v_add_u32_e32 v2, s36, v182
	ds_read_b128 v[4:7], v2
	ds_read_b128 v[8:11], v2 offset:4096
	s_waitcnt lgkmcnt(0)
	v_mfma_f32_32x32x16_bf16 v[98:113], v[4:7], v[118:121], v[66:81]
	v_add_u32_e32 v2, s36, v184
	s_cmp_lt_u32 s55, 6
	v_mfma_f32_32x32x16_bf16 v[82:97], v[8:11], v[118:121], v[66:81]
	ds_read_b128 v[4:7], v2
	ds_read_b128 v[8:11], v2 offset:4096
	v_add_u32_e32 v2, s36, v186
	s_waitcnt lgkmcnt(0)
	v_mfma_f32_32x32x16_bf16 v[98:113], v[4:7], v[122:125], v[98:113]
	v_mfma_f32_32x32x16_bf16 v[82:97], v[8:11], v[122:125], v[82:97]
	ds_read_b128 v[4:7], v2
	ds_read_b128 v[8:11], v2 offset:4096
	v_add_u32_e32 v2, s36, v188
	ds_read_b128 v[12:15], v2
	ds_read_b128 v[192:195], v2 offset:4096
	v_add_u32_e32 v2, s36, v183
	s_waitcnt lgkmcnt(0)
	v_mfma_f32_32x32x16_bf16 v[98:113], v[4:7], v[126:129], v[98:113]
	ds_read_b128 v[150:153], v2
	ds_read_b128 v[4:7], v2 offset:4096
	v_add_u32_e32 v2, s36, v185
	v_mfma_f32_32x32x16_bf16 v[82:97], v[8:11], v[126:129], v[82:97]
	ds_read_b128 v[146:149], v2
	ds_read_b128 v[8:11], v2 offset:4096
	v_add_u32_e32 v2, s36, v187
	v_mfma_f32_32x32x16_bf16 v[98:113], v[12:15], v[130:133], v[98:113]
	ds_read_b128 v[142:145], v2
	ds_read_b128 v[12:15], v2 offset:4096
	v_add_u32_e32 v2, s36, v189
	ds_read_b128 v[138:141], v2
	ds_read_b128 v[134:137], v2 offset:4096
	v_mfma_f32_32x32x16_bf16 v[82:97], v[192:195], v[130:133], v[82:97]
	s_cbranch_scc1 .LBB5_988
	v_mov_b32_e32 v2, v190
	ds_read2_b32 v[200:201], v2 offset0:54 offset1:55
	ds_read2_b32 v[214:215], v2 offset0:22 offset1:23
	ds_read2_b32 v[216:217], v2 offset0:52 offset1:53
	ds_read2_b32 v[218:219], v2 offset0:20 offset1:21
	ds_read2_b32 v[220:221], v2 offset0:50 offset1:51
	ds_read2_b32 v[222:223], v2 offset0:18 offset1:19
	ds_read2_b32 v[224:225], v2 offset0:48 offset1:49
	ds_read2_b32 v[226:227], v2 offset0:16 offset1:17
	ds_read2_b32 v[228:229], v2 offset0:38 offset1:39
	ds_read2_b32 v[230:231], v2 offset0:6 offset1:7
	ds_read2_b32 v[232:233], v2 offset0:36 offset1:37
	ds_read2_b32 v[234:235], v2 offset0:4 offset1:5
	ds_read2_b32 v[236:237], v2 offset0:34 offset1:35
	ds_read2_b32 v[238:239], v2 offset0:2 offset1:3
	ds_read2_b32 v[240:241], v2 offset0:32 offset1:33
	ds_read2_b32 v[242:243], v2 offset1:1
	s_waitcnt lgkmcnt(12)
	v_pk_add_f32 v[98:99], v[98:99], v[200:201] op_sel:[0,1] op_sel_hi:[1,0]
	s_nop 2
	v_pk_add_f32 v[82:83], v[82:83], v[214:215] op_sel:[0,1] op_sel_hi:[1,0]
	v_pk_add_f32 v[100:101], v[100:101], v[216:217] op_sel:[0,1] op_sel_hi:[1,0]
	s_waitcnt lgkmcnt(8)
	v_pk_add_f32 v[102:103], v[102:103], v[220:221] op_sel:[0,1] op_sel_hi:[1,0]
	v_pk_add_f32 v[84:85], v[84:85], v[218:219] op_sel:[0,1] op_sel_hi:[1,0]
	v_pk_add_f32 v[86:87], v[86:87], v[222:223] op_sel:[0,1] op_sel_hi:[1,0]
	v_pk_add_f32 v[104:105], v[104:105], v[224:225] op_sel:[0,1] op_sel_hi:[1,0]
	v_pk_add_f32 v[88:89], v[88:89], v[226:227] op_sel:[0,1] op_sel_hi:[1,0]
	s_waitcnt lgkmcnt(4)
	v_pk_add_f32 v[106:107], v[106:107], v[228:229] op_sel:[0,1] op_sel_hi:[1,0]
	v_pk_add_f32 v[90:91], v[90:91], v[230:231] op_sel:[0,1] op_sel_hi:[1,0]
	v_pk_add_f32 v[108:109], v[108:109], v[232:233] op_sel:[0,1] op_sel_hi:[1,0]
	v_pk_add_f32 v[92:93], v[92:93], v[234:235] op_sel:[0,1] op_sel_hi:[1,0]
	s_waitcnt lgkmcnt(0)
	v_pk_add_f32 v[110:111], v[110:111], v[236:237] op_sel:[0,1] op_sel_hi:[1,0]
	v_pk_add_f32 v[94:95], v[94:95], v[238:239] op_sel:[0,1] op_sel_hi:[1,0]
	v_pk_add_f32 v[112:113], v[112:113], v[240:241] op_sel:[0,1] op_sel_hi:[1,0]
	v_pk_add_f32 v[96:97], v[96:97], v[242:243] op_sel:[0,1] op_sel_hi:[1,0]
